# speedup vs baseline: 1.0015x; 1.0011x over previous
.LBB1_3:
	ds_read_b128 v[128:131], v126 offset:49152
	ds_read_b128 v[132:135], v126 offset:50176
	ds_read_b128 v[136:139], v126 offset:51200
	ds_read_b128 v[140:143], v126 offset:52224
	s_add_u32 s30, s16, s0
	s_addc_u32 s31, s17, s1
	ds_read_b128 v[144:147], v110
	ds_read_b128 v[148:151], v110 offset:1024
	ds_read_b128 v[152:155], v109
	ds_read_b128 v[156:159], v109 offset:1024
	ds_read_b128 v[160:163], v108
	ds_read_b128 v[164:167], v108 offset:1024
	v_readfirstlane_b32 s34, v127
	s_add_u32 s52, s30, s18
	s_addc_u32 s53, s31, s19
	s_mov_b32 m0, s34
	s_nop 0
	global_load_lds_dwordx4 v100, s[52:53]
	v_readfirstlane_b32 s34, v125
	s_mov_b32 m0, s34
	s_nop 0
	global_load_lds_dwordx4 v101, s[52:53]
	s_waitcnt lgkmcnt(6)
	s_barrier
	s_waitcnt lgkmcnt(0)
	s_setprio 0
	s_waitcnt lgkmcnt(0)
	v_mfma_f32_16x16x32_f16 v[94:97], v[144:147], v[128:131], v[94:97]
	v_mfma_f32_16x16x32_f16 v[90:93], v[144:147], v[136:139], v[90:93]
	v_mfma_f32_16x16x32_f16 v[86:89], v[152:155], v[128:131], v[86:89]
	v_mfma_f32_16x16x32_f16 v[82:85], v[152:155], v[136:139], v[82:85]
	v_mfma_f32_16x16x32_f16 v[78:81], v[160:163], v[128:131], v[78:81]
	v_mfma_f32_16x16x32_f16 v[74:77], v[160:163], v[136:139], v[74:77]
	v_mfma_f32_16x16x32_f16 v[94:97], v[148:151], v[132:135], v[94:97]
	v_mfma_f32_16x16x32_f16 v[90:93], v[148:151], v[140:143], v[90:93]
	v_mfma_f32_16x16x32_f16 v[86:89], v[156:159], v[132:135], v[86:89]
	v_mfma_f32_16x16x32_f16 v[82:85], v[156:159], v[140:143], v[82:85]
	v_mfma_f32_16x16x32_f16 v[78:81], v[164:167], v[132:135], v[78:81]
	v_mfma_f32_16x16x32_f16 v[74:77], v[164:167], v[140:143], v[74:77]
	s_setprio 1
	s_barrier
	s_add_u32 s34, s2, s0
	s_addc_u32 s35, s3, s1
	ds_read_b128 v[168:171], v122
	ds_read_b128 v[172:175], v122 offset:1024
	ds_read_b128 v[176:179], v122 offset:2048
	ds_read_b128 v[180:183], v122 offset:3072
	v_readfirstlane_b32 s42, v106
	s_add_u32 s54, s34, s20
	s_addc_u32 s55, s35, s21
	s_mov_b32 m0, s42
	s_nop 0
	global_load_lds_dwordx4 v100, s[54:55]
	v_readfirstlane_b32 s42, v107
	s_mov_b32 m0, s42
	s_nop 0
	global_load_lds_dwordx4 v103, s[54:55]
	s_barrier
	s_waitcnt lgkmcnt(0)
	s_setprio 0
	s_waitcnt lgkmcnt(0)
	v_mfma_f32_16x16x32_f16 v[70:73], v[144:147], v[168:171], v[70:73]
	v_mfma_f32_16x16x32_f16 v[66:69], v[144:147], v[176:179], v[66:69]
	v_mfma_f32_16x16x32_f16 v[62:65], v[152:155], v[168:171], v[62:65]
	v_mfma_f32_16x16x32_f16 v[50:53], v[152:155], v[176:179], v[50:53]
	v_mfma_f32_16x16x32_f16 v[46:49], v[160:163], v[168:171], v[46:49]
	v_mfma_f32_16x16x32_f16 v[42:45], v[160:163], v[176:179], v[42:45]
	v_mfma_f32_16x16x32_f16 v[70:73], v[148:151], v[172:175], v[70:73]
	v_mfma_f32_16x16x32_f16 v[66:69], v[148:151], v[180:183], v[66:69]
	v_mfma_f32_16x16x32_f16 v[62:65], v[156:159], v[172:175], v[62:65]
	v_mfma_f32_16x16x32_f16 v[50:53], v[156:159], v[180:183], v[50:53]
	v_mfma_f32_16x16x32_f16 v[46:49], v[164:167], v[172:175], v[46:49]
	v_mfma_f32_16x16x32_f16 v[42:45], v[164:167], v[180:183], v[42:45]
	s_setprio 1
	s_barrier
	ds_read_b128 v[144:147], v110 offset:12288
	ds_read_b128 v[148:151], v110 offset:13312
	ds_read_b128 v[152:155], v109 offset:12288
	ds_read_b128 v[156:159], v109 offset:13312
	ds_read_b128 v[160:163], v108 offset:12288
	ds_read_b128 v[164:167], v108 offset:13312
	v_readfirstlane_b32 s42, v1
	s_add_u32 s54, s30, s20
	s_addc_u32 s55, s31, s21
	s_mov_b32 m0, s42
	s_nop 0
	global_load_lds_dwordx4 v100, s[54:55]
	v_readfirstlane_b32 s42, v111
	s_mov_b32 m0, s42
	s_nop 0
	global_load_lds_dwordx4 v101, s[54:55]
	s_barrier
	s_waitcnt lgkmcnt(0)
	s_setprio 0
	s_waitcnt lgkmcnt(0)
	v_mfma_f32_16x16x32_f16 v[38:41], v[144:147], v[128:131], v[38:41]
	v_mfma_f32_16x16x32_f16 v[34:37], v[144:147], v[136:139], v[34:37]
	v_mfma_f32_16x16x32_f16 v[30:33], v[152:155], v[128:131], v[30:33]
	v_mfma_f32_16x16x32_f16 v[26:29], v[152:155], v[136:139], v[26:29]
	v_mfma_f32_16x16x32_f16 v[22:25], v[160:163], v[128:131], v[22:25]
	v_mfma_f32_16x16x32_f16 v[18:21], v[160:163], v[136:139], v[18:21]
	v_mfma_f32_16x16x32_f16 v[38:41], v[148:151], v[132:135], v[38:41]
	v_mfma_f32_16x16x32_f16 v[34:37], v[148:151], v[140:143], v[34:37]
	v_mfma_f32_16x16x32_f16 v[30:33], v[156:159], v[132:135], v[30:33]
	v_mfma_f32_16x16x32_f16 v[26:29], v[156:159], v[140:143], v[26:29]
	v_mfma_f32_16x16x32_f16 v[22:25], v[164:167], v[132:135], v[22:25]
	v_mfma_f32_16x16x32_f16 v[18:21], v[164:167], v[140:143], v[18:21]
	s_setprio 1
	s_barrier
	v_readfirstlane_b32 s42, v112
	s_add_u32 s56, s34, s22
	s_addc_u32 s57, s35, s23
	s_mov_b32 m0, s42
	s_nop 0
	global_load_lds_dwordx4 v100, s[56:57]
	v_readfirstlane_b32 s42, v113
	s_mov_b32 m0, s42
	s_nop 0
	global_load_lds_dwordx4 v103, s[56:57]
	s_waitcnt vmcnt(6)
	s_barrier
	s_setprio 0
	v_mfma_f32_16x16x32_f16 v[14:17], v[144:147], v[168:171], v[14:17]
	v_mfma_f32_16x16x32_f16 v[10:13], v[144:147], v[176:179], v[10:13]
	v_mfma_f32_16x16x32_f16 v[6:9], v[152:155], v[168:171], v[6:9]
	v_mfma_f32_16x16x32_f16 v[2:5], v[152:155], v[176:179], v[2:5]
	v_mfma_f32_16x16x32_f16 v[54:57], v[160:163], v[168:171], v[54:57]
	v_mfma_f32_16x16x32_f16 v[58:61], v[160:163], v[176:179], v[58:61]
	v_mfma_f32_16x16x32_f16 v[14:17], v[148:151], v[172:175], v[14:17]
	v_mfma_f32_16x16x32_f16 v[10:13], v[148:151], v[180:183], v[10:13]
	v_mfma_f32_16x16x32_f16 v[6:9], v[156:159], v[172:175], v[6:9]
	v_mfma_f32_16x16x32_f16 v[2:5], v[156:159], v[180:183], v[2:5]
	v_mfma_f32_16x16x32_f16 v[54:57], v[164:167], v[172:175], v[54:57]
	v_mfma_f32_16x16x32_f16 v[58:61], v[164:167], v[180:183], v[58:61]
	s_setprio 1
	s_barrier
	ds_read_b128 v[128:131], v117
	ds_read_b128 v[132:135], v117 offset:1024
	ds_read_b128 v[136:139], v117 offset:2048
	ds_read_b128 v[140:143], v117 offset:3072
	ds_read_b128 v[144:147], v110 offset:24576
	ds_read_b128 v[148:151], v110 offset:25600
	ds_read_b128 v[152:155], v109 offset:24576
	ds_read_b128 v[156:159], v109 offset:25600
	ds_read_b128 v[160:163], v108 offset:24576
	ds_read_b128 v[164:167], v108 offset:25600
	v_readfirstlane_b32 s42, v115
	s_add_u32 s52, s30, s24
	s_addc_u32 s53, s31, s25
	s_mov_b32 m0, s42
	s_nop 0
	global_load_lds_dwordx4 v100, s[52:53]
	v_readfirstlane_b32 s42, v116
	s_mov_b32 m0, s42
	s_nop 0
	global_load_lds_dwordx4 v101, s[52:53]
	s_waitcnt lgkmcnt(6)
	s_barrier
	s_waitcnt lgkmcnt(0)
	s_setprio 0
	s_waitcnt lgkmcnt(0)
	v_mfma_f32_16x16x32_f16 v[94:97], v[144:147], v[128:131], v[94:97]
	v_mfma_f32_16x16x32_f16 v[90:93], v[144:147], v[136:139], v[90:93]
	v_mfma_f32_16x16x32_f16 v[86:89], v[152:155], v[128:131], v[86:89]
	v_mfma_f32_16x16x32_f16 v[82:85], v[152:155], v[136:139], v[82:85]
	v_mfma_f32_16x16x32_f16 v[78:81], v[160:163], v[128:131], v[78:81]
	v_mfma_f32_16x16x32_f16 v[74:77], v[160:163], v[136:139], v[74:77]
	v_mfma_f32_16x16x32_f16 v[94:97], v[148:151], v[132:135], v[94:97]
	v_mfma_f32_16x16x32_f16 v[90:93], v[148:151], v[140:143], v[90:93]
	v_mfma_f32_16x16x32_f16 v[86:89], v[156:159], v[132:135], v[86:89]
	v_mfma_f32_16x16x32_f16 v[82:85], v[156:159], v[140:143], v[82:85]
	v_mfma_f32_16x16x32_f16 v[78:81], v[164:167], v[132:135], v[78:81]
	v_mfma_f32_16x16x32_f16 v[74:77], v[164:167], v[140:143], v[74:77]
	s_setprio 1
	s_barrier
	ds_read_b128 v[168:171], v114
	ds_read_b128 v[172:175], v114 offset:1024
	ds_read_b128 v[176:179], v114 offset:2048
	ds_read_b128 v[180:183], v114 offset:3072
	v_readfirstlane_b32 s42, v118
	s_add_u32 s54, s34, s26
	s_addc_u32 s55, s35, s27
	s_mov_b32 m0, s42
	s_nop 0
	global_load_lds_dwordx4 v100, s[54:55]
	v_readfirstlane_b32 s42, v119
	s_mov_b32 m0, s42
	s_nop 0
	global_load_lds_dwordx4 v103, s[54:55]
	s_barrier
	s_waitcnt lgkmcnt(0)
	s_setprio 0
	s_waitcnt lgkmcnt(0)
	v_mfma_f32_16x16x32_f16 v[70:73], v[144:147], v[168:171], v[70:73]
	v_mfma_f32_16x16x32_f16 v[66:69], v[144:147], v[176:179], v[66:69]
	v_mfma_f32_16x16x32_f16 v[62:65], v[152:155], v[168:171], v[62:65]
	v_mfma_f32_16x16x32_f16 v[50:53], v[152:155], v[176:179], v[50:53]
	v_mfma_f32_16x16x32_f16 v[46:49], v[160:163], v[168:171], v[46:49]
	v_mfma_f32_16x16x32_f16 v[42:45], v[160:163], v[176:179], v[42:45]
	v_mfma_f32_16x16x32_f16 v[70:73], v[148:151], v[172:175], v[70:73]
	v_mfma_f32_16x16x32_f16 v[66:69], v[148:151], v[180:183], v[66:69]
	v_mfma_f32_16x16x32_f16 v[62:65], v[156:159], v[172:175], v[62:65]
	v_mfma_f32_16x16x32_f16 v[50:53], v[156:159], v[180:183], v[50:53]
	v_mfma_f32_16x16x32_f16 v[46:49], v[164:167], v[172:175], v[46:49]
	v_mfma_f32_16x16x32_f16 v[42:45], v[164:167], v[180:183], v[42:45]
	s_setprio 1
	s_barrier
	ds_read_b128 v[144:147], v110 offset:36864
	ds_read_b128 v[148:151], v110 offset:37888
	ds_read_b128 v[152:155], v109 offset:36864
	ds_read_b128 v[156:159], v109 offset:37888
	ds_read_b128 v[160:163], v108 offset:36864
	ds_read_b128 v[164:167], v108 offset:37888
	v_readfirstlane_b32 s42, v120
	s_add_u32 s54, s30, s26
	s_addc_u32 s55, s31, s27
	s_mov_b32 m0, s42
	s_nop 0
	global_load_lds_dwordx4 v100, s[54:55]
	s_nop 0
	v_readfirstlane_b32 s30, v121
	s_mov_b32 m0, s30
	s_nop 0
	global_load_lds_dwordx4 v101, s[54:55]
	s_barrier
	s_waitcnt lgkmcnt(0)
	s_setprio 0
	s_waitcnt lgkmcnt(0)
	v_mfma_f32_16x16x32_f16 v[38:41], v[144:147], v[128:131], v[38:41]
	v_mfma_f32_16x16x32_f16 v[34:37], v[144:147], v[136:139], v[34:37]
	v_mfma_f32_16x16x32_f16 v[30:33], v[152:155], v[128:131], v[30:33]
	v_mfma_f32_16x16x32_f16 v[26:29], v[152:155], v[136:139], v[26:29]
	v_mfma_f32_16x16x32_f16 v[22:25], v[160:163], v[128:131], v[22:25]
	v_mfma_f32_16x16x32_f16 v[18:21], v[160:163], v[136:139], v[18:21]
	v_mfma_f32_16x16x32_f16 v[38:41], v[148:151], v[132:135], v[38:41]
	v_mfma_f32_16x16x32_f16 v[34:37], v[148:151], v[140:143], v[34:37]
	v_mfma_f32_16x16x32_f16 v[30:33], v[156:159], v[132:135], v[30:33]
	v_mfma_f32_16x16x32_f16 v[26:29], v[156:159], v[140:143], v[26:29]
	v_mfma_f32_16x16x32_f16 v[22:25], v[164:167], v[132:135], v[22:25]
	v_mfma_f32_16x16x32_f16 v[18:21], v[164:167], v[140:143], v[18:21]
	s_setprio 1
	s_barrier
	v_readfirstlane_b32 s30, v123
	s_add_u32 s56, s34, s28
	s_addc_u32 s57, s35, s29
	s_mov_b32 m0, s30
	s_nop 0
	global_load_lds_dwordx4 v100, s[56:57]
	v_readfirstlane_b32 s30, v124
	s_mov_b32 m0, s30
	s_nop 0
	global_load_lds_dwordx4 v103, s[56:57]
	s_waitcnt vmcnt(6)
	s_barrier
	s_setprio 0
	v_mfma_f32_16x16x32_f16 v[14:17], v[144:147], v[168:171], v[14:17]
	v_mfma_f32_16x16x32_f16 v[10:13], v[144:147], v[176:179], v[10:13]
	v_mfma_f32_16x16x32_f16 v[6:9], v[152:155], v[168:171], v[6:9]
	v_mfma_f32_16x16x32_f16 v[2:5], v[152:155], v[176:179], v[2:5]
	v_mfma_f32_16x16x32_f16 v[54:57], v[160:163], v[168:171], v[54:57]
	v_mfma_f32_16x16x32_f16 v[58:61], v[160:163], v[176:179], v[58:61]
	v_mfma_f32_16x16x32_f16 v[14:17], v[148:151], v[172:175], v[14:17]
	v_mfma_f32_16x16x32_f16 v[10:13], v[148:151], v[180:183], v[10:13]
	v_mfma_f32_16x16x32_f16 v[6:9], v[156:159], v[172:175], v[6:9]
	v_mfma_f32_16x16x32_f16 v[2:5], v[156:159], v[180:183], v[2:5]
	v_mfma_f32_16x16x32_f16 v[54:57], v[164:167], v[172:175], v[54:57]
	v_mfma_f32_16x16x32_f16 v[58:61], v[164:167], v[180:183], v[58:61]
	s_setprio 1
	s_add_i32 s41, s41, 2
	s_add_u32 s0, s0, 0x100
	s_addc_u32 s1, s1, 0
	s_cmp_lt_u32 s41, 12
	s_barrier
	s_cbranch_scc1 .LBB1_3
	v_add_u32_e32 v98, 0x9000, v1
	s_add_u32 s0, s16, 0x30780
	v_readfirstlane_b32 s2, v98
	s_addc_u32 s1, s17, 0
	s_mov_b32 m0, s2
	v_readfirstlane_b32 s2, v125
	ds_read_b128 v[118:121], v126 offset:49152
	ds_read_b128 v[128:131], v126 offset:50176
	ds_read_b128 v[132:135], v126 offset:51200
	ds_read_b128 v[136:139], v126 offset:52224
	ds_read_b128 v[140:143], v110
	ds_read_b128 v[144:147], v110 offset:1024
	ds_read_b128 v[148:151], v109
	ds_read_b128 v[152:155], v109 offset:1024
	ds_read_b128 v[156:159], v108
	ds_read_b128 v[160:163], v108 offset:1024
	s_nop 0
	global_load_lds_dwordx4 v100, s[0:1]
	s_mov_b32 m0, s2
	s_nop 0
	global_load_lds_dwordx4 v101, s[0:1]
	s_barrier
	s_waitcnt lgkmcnt(0)
	s_setprio 0
	s_waitcnt lgkmcnt(0)
	v_mfma_f32_16x16x32_f16 v[90:93], v[140:143], v[132:135], v[90:93]
	v_mfma_f32_16x16x32_f16 v[86:89], v[148:151], v[118:121], v[86:89]
	v_mfma_f32_16x16x32_f16 v[82:85], v[148:151], v[132:135], v[82:85]
	v_mfma_f32_16x16x32_f16 v[94:97], v[140:143], v[118:121], v[94:97]
	v_mfma_f32_16x16x32_f16 v[90:93], v[144:147], v[136:139], v[90:93]
	v_mfma_f32_16x16x32_f16 v[86:89], v[152:155], v[128:131], v[86:89]
	v_mfma_f32_16x16x32_f16 v[82:85], v[152:155], v[136:139], v[82:85]
	v_mfma_f32_16x16x32_f16 v[78:81], v[156:159], v[118:121], v[78:81]
	v_mfma_f32_16x16x32_f16 v[74:77], v[156:159], v[132:135], v[74:77]
	v_mfma_f32_16x16x32_f16 v[94:97], v[144:147], v[128:131], v[94:97]
	v_mfma_f32_16x16x32_f16 v[124:127], v[160:163], v[128:131], v[78:81]
	v_mfma_f32_16x16x32_f16 v[164:167], v[160:163], v[136:139], v[74:77]
	s_setprio 1
	s_barrier
	s_nop 2
	ds_read_b128 v[74:77], v122
	ds_read_b128 v[78:81], v122 offset:1024
	ds_read_b128 v[98:101], v122 offset:2048
	ds_read_b128 v[168:171], v122 offset:3072
	s_barrier
	s_waitcnt lgkmcnt(0)
	s_setprio 0
	s_waitcnt lgkmcnt(0)
	v_mfma_f32_16x16x32_f16 v[70:73], v[140:143], v[74:77], v[70:73]
	v_mfma_f32_16x16x32_f16 v[66:69], v[140:143], v[98:101], v[66:69]
	v_mfma_f32_16x16x32_f16 v[50:53], v[148:151], v[98:101], v[50:53]
	v_mfma_f32_16x16x32_f16 v[46:49], v[156:159], v[74:77], v[46:49]
	v_mfma_f32_16x16x32_f16 v[42:45], v[156:159], v[98:101], v[42:45]
	v_mfma_f32_16x16x32_f16 v[70:73], v[144:147], v[78:81], v[70:73]
	v_mfma_f32_16x16x32_f16 v[66:69], v[144:147], v[168:171], v[66:69]
	v_mfma_f32_16x16x32_f16 v[62:65], v[148:151], v[74:77], v[62:65]
	v_mfma_f32_16x16x32_f16 v[50:53], v[152:155], v[168:171], v[50:53]
	v_mfma_f32_16x16x32_f16 v[46:49], v[160:163], v[78:81], v[46:49]
	v_mfma_f32_16x16x32_f16 v[42:45], v[160:163], v[168:171], v[42:45]
	v_mfma_f32_16x16x32_f16 v[140:143], v[152:155], v[78:81], v[62:65]
	s_setprio 1
	s_barrier
	s_nop 1
	ds_read_b128 v[62:65], v110 offset:12288
	ds_read_b128 v[144:147], v110 offset:13312
	ds_read_b128 v[148:151], v109 offset:12288
	ds_read_b128 v[152:155], v109 offset:13312
	ds_read_b128 v[156:159], v108 offset:12288
	ds_read_b128 v[160:163], v108 offset:13312
	s_waitcnt vmcnt(4)
	s_barrier
	s_waitcnt lgkmcnt(0)
	s_setprio 0
	s_waitcnt lgkmcnt(0)
	v_mfma_f32_16x16x32_f16 v[38:41], v[62:65], v[118:121], v[38:41]
	v_mfma_f32_16x16x32_f16 v[34:37], v[62:65], v[132:135], v[34:37]
	v_mfma_f32_16x16x32_f16 v[30:33], v[148:151], v[118:121], v[30:33]
	v_mfma_f32_16x16x32_f16 v[26:29], v[148:151], v[132:135], v[26:29]
	v_mfma_f32_16x16x32_f16 v[22:25], v[156:159], v[118:121], v[22:25]
	v_mfma_f32_16x16x32_f16 v[18:21], v[156:159], v[132:135], v[18:21]
	v_mfma_f32_16x16x32_f16 v[38:41], v[144:147], v[128:131], v[38:41]
	v_mfma_f32_16x16x32_f16 v[34:37], v[144:147], v[136:139], v[34:37]
	v_mfma_f32_16x16x32_f16 v[30:33], v[152:155], v[128:131], v[30:33]
	v_mfma_f32_16x16x32_f16 v[26:29], v[152:155], v[136:139], v[26:29]
	v_mfma_f32_16x16x32_f16 v[22:25], v[160:163], v[128:131], v[22:25]
	v_mfma_f32_16x16x32_f16 v[18:21], v[160:163], v[136:139], v[18:21]
	s_setprio 1
	s_setprio 0
	v_mfma_f32_16x16x32_f16 v[10:13], v[62:65], v[98:101], v[10:13]
	v_mfma_f32_16x16x32_f16 v[128:131], v[144:147], v[168:171], v[10:13]
	v_mfma_f32_16x16x32_f16 v[6:9], v[148:151], v[74:77], v[6:9]
	v_mfma_f32_16x16x32_f16 v[2:5], v[148:151], v[98:101], v[2:5]
	v_mfma_f32_16x16x32_f16 v[10:13], v[156:159], v[74:77], v[54:57]
	v_mfma_f32_16x16x32_f16 v[14:17], v[62:65], v[74:77], v[14:17]
	v_mfma_f32_16x16x32_f16 v[6:9], v[152:155], v[78:81], v[6:9]
	v_mfma_f32_16x16x32_f16 v[2:5], v[152:155], v[168:171], v[2:5]
	v_mfma_f32_16x16x32_f16 v[132:135], v[160:163], v[78:81], v[10:13]
	v_mfma_f32_16x16x32_f16 v[10:13], v[156:159], v[98:101], v[58:61]
	v_mfma_f32_16x16x32_f16 v[118:121], v[144:147], v[78:81], v[14:17]
	v_mfma_f32_16x16x32_f16 v[136:139], v[160:163], v[168:171], v[10:13]
	s_setprio 1
	s_barrier
	s_nop 3
	ds_read_b128 v[10:13], v117
	ds_read_b128 v[14:17], v117 offset:1024
	ds_read_b128 v[144:147], v117 offset:2048
	ds_read_b128 v[148:151], v117 offset:3072
	ds_read_b128 v[54:57], v110 offset:24576
	ds_read_b128 v[152:155], v110 offset:25600
	ds_read_b128 v[156:159], v109 offset:24576
	ds_read_b128 v[160:163], v109 offset:25600
	ds_read_b128 v[168:171], v108 offset:24576
	ds_read_b128 v[172:175], v108 offset:25600
	s_waitcnt vmcnt(2)
	s_barrier
	s_waitcnt lgkmcnt(0)
	s_setprio 0
	s_waitcnt lgkmcnt(0)
	v_mfma_f32_16x16x32_f16 v[58:61], v[54:57], v[10:13], v[94:97]
	v_mfma_f32_16x16x32_f16 v[98:101], v[152:155], v[14:17], v[58:61]
	v_mfma_f32_16x16x32_f16 v[58:61], v[54:57], v[144:147], v[90:93]
	v_mfma_f32_16x16x32_f16 v[90:93], v[152:155], v[148:151], v[58:61]
	v_mfma_f32_16x16x32_f16 v[58:61], v[156:159], v[10:13], v[86:89]
	v_mfma_f32_16x16x32_f16 v[78:81], v[160:163], v[14:17], v[58:61]
	v_mfma_f32_16x16x32_f16 v[58:61], v[156:159], v[144:147], v[82:85]
	v_mfma_f32_16x16x32_f16 v[74:77], v[160:163], v[148:151], v[58:61]
	v_mfma_f32_16x16x32_f16 v[58:61], v[168:171], v[10:13], v[124:127]
	v_mfma_f32_16x16x32_f16 v[62:65], v[172:175], v[14:17], v[58:61]
	v_mfma_f32_16x16x32_f16 v[58:61], v[168:171], v[144:147], v[164:167]
	v_mfma_f32_16x16x32_f16 v[58:61], v[172:175], v[148:151], v[58:61]
	s_setprio 1
	s_barrier
	ds_read_b128 v[94:97], v114
	ds_read_b128 v[122:125], v114 offset:1024
	ds_read_b128 v[164:167], v114 offset:2048
	ds_read_b128 v[112:115], v114 offset:3072
	s_waitcnt vmcnt(0)
	s_barrier
	s_waitcnt lgkmcnt(0)
	s_setprio 0
	s_waitcnt lgkmcnt(0)
	v_mfma_f32_16x16x32_f16 v[70:73], v[54:57], v[94:97], v[70:73]
	v_mfma_f32_16x16x32_f16 v[54:57], v[54:57], v[164:167], v[66:69]
	v_mfma_f32_16x16x32_f16 v[82:85], v[152:155], v[112:115], v[54:57]
	v_mfma_f32_16x16x32_f16 v[54:57], v[156:159], v[94:97], v[140:143]
	v_mfma_f32_16x16x32_f16 v[50:53], v[156:159], v[164:167], v[50:53]
	v_mfma_f32_16x16x32_f16 v[46:49], v[168:171], v[94:97], v[46:49]
	v_mfma_f32_16x16x32_f16 v[42:45], v[168:171], v[164:167], v[42:45]
	v_mfma_f32_16x16x32_f16 v[86:89], v[152:155], v[122:125], v[70:73]
	v_mfma_f32_16x16x32_f16 v[70:73], v[160:163], v[122:125], v[54:57]
	v_mfma_f32_16x16x32_f16 v[66:69], v[160:163], v[112:115], v[50:53]
	v_mfma_f32_16x16x32_f16 v[54:57], v[172:175], v[122:125], v[46:49]
	v_mfma_f32_16x16x32_f16 v[50:53], v[172:175], v[112:115], v[42:45]
	s_setprio 1
	s_barrier
	ds_read_b128 v[140:143], v110 offset:36864
	ds_read_b128 v[152:155], v110 offset:37888
	ds_read_b128 v[156:159], v109 offset:36864
	ds_read_b128 v[160:163], v109 offset:37888
	ds_read_b128 v[168:171], v108 offset:36864
	ds_read_b128 v[106:109], v108 offset:37888
	s_barrier
	s_waitcnt lgkmcnt(0)
	s_setprio 0
	s_waitcnt lgkmcnt(0)
	v_mfma_f32_16x16x32_f16 v[38:41], v[140:143], v[10:13], v[38:41]
	v_mfma_f32_16x16x32_f16 v[30:33], v[156:159], v[10:13], v[30:33]
	v_mfma_f32_16x16x32_f16 v[10:13], v[168:171], v[10:13], v[22:25]
	v_mfma_f32_16x16x32_f16 v[46:49], v[152:155], v[14:17], v[38:41]
	v_mfma_f32_16x16x32_f16 v[34:37], v[140:143], v[144:147], v[34:37]
	v_mfma_f32_16x16x32_f16 v[30:33], v[160:163], v[14:17], v[30:33]
	v_mfma_f32_16x16x32_f16 v[26:29], v[156:159], v[144:147], v[26:29]
	v_mfma_f32_16x16x32_f16 v[14:17], v[106:109], v[14:17], v[10:13]
	v_mfma_f32_16x16x32_f16 v[10:13], v[168:171], v[144:147], v[18:21]
	v_mfma_f32_16x16x32_f16 v[42:45], v[152:155], v[148:151], v[34:37]
	v_mfma_f32_16x16x32_f16 v[26:29], v[160:163], v[148:151], v[26:29]
	v_mfma_f32_16x16x32_f16 v[10:13], v[106:109], v[148:151], v[10:13]
	s_setprio 1
	s_setprio 0
	v_mfma_f32_16x16x32_f16 v[18:21], v[140:143], v[94:97], v[118:121]
	v_mfma_f32_16x16x32_f16 v[38:41], v[152:155], v[122:125], v[18:21]
	v_mfma_f32_16x16x32_f16 v[18:21], v[140:143], v[164:167], v[128:131]
	v_mfma_f32_16x16x32_f16 v[2:5], v[156:159], v[164:167], v[2:5]
	v_mfma_f32_16x16x32_f16 v[34:37], v[152:155], v[112:115], v[18:21]
	v_mfma_f32_16x16x32_f16 v[6:9], v[156:159], v[94:97], v[6:9]
	v_mfma_f32_16x16x32_f16 v[18:21], v[160:163], v[112:115], v[2:5]
	v_mfma_f32_16x16x32_f16 v[2:5], v[168:171], v[94:97], v[132:135]
	v_mfma_f32_16x16x32_f16 v[22:25], v[160:163], v[122:125], v[6:9]
	v_mfma_f32_16x16x32_f16 v[6:9], v[106:109], v[122:125], v[2:5]
	v_mfma_f32_16x16x32_f16 v[2:5], v[168:171], v[164:167], v[136:139]
	v_mfma_f32_16x16x32_f16 v[2:5], v[106:109], v[112:115], v[2:5]
	s_setprio 1
	s_andn2_b64 vcc, exec, vcc
	s_barrier
	s_cbranch_vccnz .LBB1_6
	s_barrier
